# spatial-gating unit: the four serialized LayerNorm-input row loads issued together (one round trip instead of four); gate-operand LDS reads deferred to just before the staging barrier
# speedup vs baseline: 1.0020x; 1.0020x over previous
; __device__ __forceinline__ int crow(int r, int hi) { return (r & 3) + 8 * (r >> 2) + 4 * hi; }
; __device__ __forceinline__ void unit(const bf16_t* proj, const float* stats  , const float* lng, const float* lnb, const float* sw, const float* sb, bf16_t* Y2, int un, LAS unsigned char* lds) {
;     ...
;     f32x4 wv[16]; unsigned uu[32], zq[32]; float bias[16];
; #pragma unroll
;     for (int i = 0; i < 8; ++i) { const int s0 = (i >> 2) * 64 + 16 * (i & 3) + hi * 8; const float* wp = sw + ((size_t)g * 128 + t) * 128 + s0; wv[2 * i] = *(const f32x4*)wp; wv[2 * i + 1] = *(const f32x4*)(wp + 4); }
; #pragma unroll
;     for (int r = 0; r < 16; ++r) { const int tr = tb * 32 + att::crow(r, hi), bt = R0 + tr; bias[r] = sb[g * 128 + tr];
; #pragma unroll
;         for (int d = 0; d < 2; ++d) { const int ch = g * 128 + (2 * eh + d) * 32 + (r32 & ~1); uu[r * 2 + d] = *(const unsigned*)(proj + (size_t)bt * NC + C_UC + ch); zq[r * 2 + d] = *(const unsigned*)(proj + (size_t)bt * NC + C_ZC + ch); } }
.LBB0_1376:
	s_andn2_b64 vcc, exec, s[0:1]
	s_cbranch_vccnz .LBB0_425
	v_readlane_b32 s4, v252, 35
	v_readlane_b32 s10, v252, 41
	v_readlane_b32 s11, v252, 42
	s_mov_b64 s[0:1], s[10:11]
	v_readlane_b32 s5, v252, 36
	v_readlane_b32 s12, v252, 43
	v_readlane_b32 s13, v252, 44
	v_readlane_b32 s10, v254, 43
	v_readlane_b32 s11, v254, 44
	s_add_u32 s0, s0, s10
	s_mov_b64 s[4:5], s[12:13]
	s_addc_u32 s1, s1, s11
	v_readlane_b32 s6, v252, 37
	v_readlane_b32 s7, v252, 38
	v_readlane_b32 s8, v252, 39
	v_readlane_b32 s9, v252, 40
	v_readlane_b32 s14, v252, 45
	v_readlane_b32 s15, v252, 46
	s_add_u32 s4, s4, s10
	s_addc_u32 s5, s5, s11
	s_mov_b64 s[6:7], s[14:15]
	v_readlane_b32 s8, v253, 54
	v_readlane_b32 s16, v252, 47
	v_readlane_b32 s17, v252, 48
	v_readlane_b32 s9, v253, 55
	s_add_u32 s12, s6, s8
	s_addc_u32 s13, s7, s9
	s_mov_b64 s[6:7], s[16:17]
	s_add_u32 s6, s6, s10
	v_readlane_b32 s8, v254, 47
	s_addc_u32 s7, s7, s11
	s_waitcnt vmcnt(23)
	v_mov_b32_e32 v176, v0
	s_and_b32 s2, s8, 7
	s_lshl_b32 s8, s8, 4
	s_add_i32 s8, s8, 0x7fffe000
	v_readfirstlane_b32 s10, v176
	s_and_b32 s11, s8, 0x7fffff80
	s_lshr_b32 s8, s10, 1
	v_and_b32_e32 v177, 31, v176
	s_and_b32 s9, s8, 0x60
	v_or_b32_e32 v182, s9, v177
	s_lshl_b32 s8, s2, 16
	s_waitcnt vmcnt(3)
	v_lshl_or_b32 v2, v182, 9, s8
	v_lshl_add_u64 v[4:5], s[12:13], 0, v[2:3]
	v_and_b32_e32 v2, 32, v176
	s_lshl_b32 s2, s2, 7
	s_ashr_i32 s8, s10, 2
	v_lshl_add_u64 v[40:41], v[4:5], 0, v[2:3]
	s_andn2_b32 s8, s8, 63
	v_and_or_b32 v2, v176, 30, s2
	s_waitcnt vmcnt(0)
	v_bfe_u32 v1, v176, 5, 1
	v_add_u32_e32 v68, s8, v2
	v_readlane_b32 s12, v253, 48
	v_lshlrev_b32_e32 v183, 3, v1
	v_lshl_or_b32 v1, v1, 2, s9
	v_ashrrev_i32_e32 v69, 31, v68
	v_readlane_b32 s13, v253, 49
	v_or_b32_e32 v2, s11, v1
	s_mov_b32 s14, 0xe800
	v_mov_b64_e32 v[100:101], s[12:13]
	v_lshlrev_b64 v[84:85], 1, v[68:69]
	v_or_b32_e32 v68, 32, v68
	v_readlane_b32 s18, v252, 49
	v_readlane_b32 s19, v252, 50
	v_mad_u64_u32 v[70:71], s[12:13], v2, s14, v[100:101]
	s_mov_b64 s[16:17], 0x4000
	v_ashrrev_i32_e32 v69, 31, v68
	v_lshl_add_u64 v[72:73], v[70:71], 0, s[16:17]
	s_mov_b64 s[18:19], 0x5000
	v_lshlrev_b64 v[86:87], 1, v[68:69]
	v_lshl_add_u64 v[70:71], v[70:71], 0, s[18:19]
	v_lshl_add_u64 v[74:75], v[72:73], 0, v[84:85]
	v_lshl_add_u64 v[68:69], v[72:73], 0, v[86:87]
	global_load_dwordx4 v[28:31], v[40:41], off offset:16
	global_load_dwordx4 v[32:35], v[40:41], off
	global_load_dwordx4 v[20:23], v[40:41], off offset:80
	global_load_dwordx4 v[24:27], v[40:41], off offset:64
	s_cmp_ge_u32 s9, 32
	s_cselect_b64 exec, -1, 0
	global_load_dwordx4 v[12:15], v[40:41], off offset:144
	global_load_dwordx4 v[16:19], v[40:41], off offset:128
	s_waitcnt lgkmcnt(0)
	global_load_dwordx4 v[4:7], v[40:41], off offset:208
	global_load_dwordx4 v[8:11], v[40:41], off offset:192
	s_cmp_ge_u32 s9, 64
	s_cselect_b64 exec, -1, 0
	global_load_dwordx4 v[60:63], v[40:41], off offset:272
	global_load_dwordx4 v[64:67], v[40:41], off offset:256
	global_load_dwordx4 v[52:55], v[40:41], off offset:336
	global_load_dwordx4 v[56:59], v[40:41], off offset:320
	s_cmp_ge_u32 s9, 0x60
	s_cselect_b64 exec, -1, 0
	global_load_dwordx4 v[44:47], v[40:41], off offset:400
	global_load_dwordx4 v[48:51], v[40:41], off offset:384
	global_load_dwordx4 v[36:39], v[40:41], off offset:464
	s_nop 0
	global_load_dwordx4 v[40:43], v[40:41], off offset:448
	s_mov_b64 exec, -1
	v_or_b32_e32 v1, s2, v1
	v_bfe_u32 v160, v176, 3, 3
	v_or_b32_e32 v160, s9, v160
	v_or_b32_e32 v160, s11, v160
	v_mad_u64_u32 v[162:163], s[12:13], v160, s14, v[100:101]
	v_and_b32_e32 v160, 7, v176
	v_lshlrev_b32_e32 v160, 4, v160
	s_add_i32 s100, s2, s8
	s_lshl_b32 s100, s100, 1
	v_add_u32_e32 v160, s100, v160
	v_mov_b32_e32 v161, 0
	v_lshl_add_u64 v[162:163], v[162:163], 0, v[160:161]
	v_lshl_add_u64 v[162:163], v[162:163], 0, s[16:17]
	s_mov_b32 s100, 0x800
	s_mov_b32 s101, 0
	v_lshl_add_u64 v[162:163], v[162:163], 0, s[100:101]
	s_mov_b32 s100, 0x74000
	global_load_dwordx4 v[120:123], v[162:163], off offset:-2048
	global_load_dwordx4 v[136:139], v[162:163], off offset:2048
	v_lshl_add_u64 v[162:163], v[162:163], 0, s[100:101]
	global_load_dwordx4 v[124:127], v[162:163], off offset:-2048
	global_load_dwordx4 v[140:143], v[162:163], off offset:2048
	v_lshl_add_u64 v[162:163], v[162:163], 0, s[100:101]
	global_load_dwordx4 v[128:131], v[162:163], off offset:-2048
	global_load_dwordx4 v[148:151], v[162:163], off offset:2048
	v_lshl_add_u64 v[162:163], v[162:163], 0, s[100:101]
	global_load_dwordx4 v[132:135], v[162:163], off offset:-2048
	global_load_dwordx4 v[152:155], v[162:163], off offset:2048
	v_lshl_add_u64 v[74:75], v[70:71], 0, v[84:85]
	v_lshl_add_u64 v[68:69], v[70:71], 0, v[86:87]
	v_or_b32_e32 v68, 1, v2
	v_mad_u64_u32 v[68:69], s[12:13], v68, s14, v[100:101]
	v_lshl_add_u64 v[70:71], v[68:69], 0, s[16:17]
	v_lshl_add_u64 v[68:69], v[68:69], 0, s[18:19]
	v_lshl_add_u64 v[72:73], v[70:71], 0, v[84:85]
	v_lshl_add_u64 v[70:71], v[70:71], 0, v[86:87]
	v_lshl_add_u64 v[72:73], v[68:69], 0, v[84:85]
	v_lshl_add_u64 v[68:69], v[68:69], 0, v[86:87]
	v_or_b32_e32 v68, 2, v2
	v_mad_u64_u32 v[68:69], s[12:13], v68, s14, v[100:101]
	v_lshl_add_u64 v[70:71], v[68:69], 0, s[16:17]
	v_lshl_add_u64 v[68:69], v[68:69], 0, s[18:19]
	v_lshl_add_u64 v[72:73], v[70:71], 0, v[84:85]
	v_lshl_add_u64 v[70:71], v[70:71], 0, v[86:87]
	v_lshl_add_u64 v[72:73], v[68:69], 0, v[84:85]
	v_lshl_add_u64 v[68:69], v[68:69], 0, v[86:87]
	v_or_b32_e32 v68, 3, v2
	v_mad_u64_u32 v[68:69], s[12:13], v68, s14, v[100:101]
	v_lshl_add_u64 v[70:71], v[68:69], 0, s[16:17]
	v_lshl_add_u64 v[68:69], v[68:69], 0, s[18:19]
; __device__ __forceinline__ int crow(int r, int hi) { return (r & 3) + 8 * (r >> 2) + 4 * hi; }
; __device__ __forceinline__ void unit(const bf16_t* proj, const float* stats  , const float* lng, const float* lnb, const float* sw, const float* sb, bf16_t* Y2, int un, LAS unsigned char* lds) {
;     ...
;     for (int r = 0; r < 16; ++r) { const int tr = tb * 32 + att::crow(r, hi), bt = R0 + tr; bias[r] = sb[g * 128 + tr];
; #pragma unroll
;         for (int d = 0; d < 2; ++d) { const int ch = g * 128 + (2 * eh + d) * 32 + (r32 & ~1); uu[r * 2 + d] = *(const unsigned*)(proj + (size_t)bt * NC + C_UC + ch); zq[r * 2 + d] = *(const unsigned*)(proj + (size_t)bt * NC + C_ZC + ch); } }
;     { const int sr = tid >> 4, sc = (tid & 15) * 8, ch = g * 128 + sc;
;       const f32x4 g0 = *(const f32x4*)(lng + ch), g1 = *(const f32x4*)(lng + ch + 4), b0 = *(const f32x4*)(lnb + ch), b1 = *(const f32x4*)(lnb + ch + 4);
;       float mus[4], rss[4];
;       { float2 pp[4];
; #pragma unroll
;         for (int q = 0; q < 4; ++q) pp[q] = *(const float2*)(stats + ((size_t)(R0 + sr + 32 * q) * 16 + (tid & 15)) * 2);
	v_lshl_add_u64 v[72:73], v[70:71], 0, v[84:85]
	v_lshl_add_u64 v[70:71], v[70:71], 0, v[86:87]
	v_lshl_add_u64 v[72:73], v[68:69], 0, v[84:85]
	v_lshl_add_u64 v[68:69], v[68:69], 0, v[86:87]
	v_or_b32_e32 v68, 8, v2
	v_mad_u64_u32 v[68:69], s[12:13], v68, s14, v[100:101]
	v_lshl_add_u64 v[70:71], v[68:69], 0, s[16:17]
	v_lshl_add_u64 v[68:69], v[68:69], 0, s[18:19]
	v_lshl_add_u64 v[72:73], v[70:71], 0, v[84:85]
	v_lshl_add_u64 v[70:71], v[70:71], 0, v[86:87]
	v_lshl_add_u64 v[72:73], v[68:69], 0, v[84:85]
	v_lshl_add_u64 v[68:69], v[68:69], 0, v[86:87]
	v_or_b32_e32 v68, 9, v2
	v_mad_u64_u32 v[68:69], s[12:13], v68, s14, v[100:101]
	v_lshl_add_u64 v[70:71], v[68:69], 0, s[16:17]
	v_lshl_add_u64 v[68:69], v[68:69], 0, s[18:19]
	v_lshl_add_u64 v[72:73], v[70:71], 0, v[84:85]
	v_lshl_add_u64 v[70:71], v[70:71], 0, v[86:87]
	v_lshl_add_u64 v[72:73], v[68:69], 0, v[84:85]
	v_lshl_add_u64 v[68:69], v[68:69], 0, v[86:87]
	v_or_b32_e32 v68, 10, v2
	v_mad_u64_u32 v[68:69], s[12:13], v68, s14, v[100:101]
	v_lshl_add_u64 v[70:71], v[68:69], 0, s[16:17]
	v_lshl_add_u64 v[68:69], v[68:69], 0, s[18:19]
	v_lshl_add_u64 v[72:73], v[70:71], 0, v[84:85]
	v_lshl_add_u64 v[70:71], v[70:71], 0, v[86:87]
	v_lshl_add_u64 v[72:73], v[68:69], 0, v[84:85]
	v_lshl_add_u64 v[68:69], v[68:69], 0, v[86:87]
	v_or_b32_e32 v68, 11, v2
	v_mad_u64_u32 v[68:69], s[12:13], v68, s14, v[100:101]
	v_lshl_add_u64 v[70:71], v[68:69], 0, s[16:17]
	v_lshl_add_u64 v[68:69], v[68:69], 0, s[18:19]
	v_lshl_add_u64 v[72:73], v[70:71], 0, v[84:85]
	v_lshl_add_u64 v[70:71], v[70:71], 0, v[86:87]
	v_lshl_add_u64 v[72:73], v[68:69], 0, v[84:85]
	v_lshl_add_u64 v[68:69], v[68:69], 0, v[86:87]
	v_or_b32_e32 v68, 16, v2
	v_mad_u64_u32 v[68:69], s[12:13], v68, s14, v[100:101]
	v_lshl_add_u64 v[70:71], v[68:69], 0, s[16:17]
	v_lshl_add_u64 v[68:69], v[68:69], 0, s[18:19]
	v_lshl_add_u64 v[88:89], v[70:71], 0, v[84:85]
	v_lshl_add_u64 v[88:89], v[68:69], 0, v[84:85]
	v_lshl_add_u64 v[70:71], v[70:71], 0, v[86:87]
	v_lshl_add_u64 v[68:69], v[68:69], 0, v[86:87]
	v_or_b32_e32 v68, 17, v2
	v_mad_u64_u32 v[68:69], s[12:13], v68, s14, v[100:101]
	v_lshl_add_u64 v[70:71], v[68:69], 0, s[16:17]
	v_lshl_add_u64 v[68:69], v[68:69], 0, s[18:19]
	v_lshl_add_u64 v[88:89], v[70:71], 0, v[84:85]
	v_lshl_add_u64 v[70:71], v[70:71], 0, v[86:87]
	v_lshl_add_u64 v[88:89], v[68:69], 0, v[84:85]
	v_lshl_add_u64 v[68:69], v[68:69], 0, v[86:87]
	v_or_b32_e32 v68, 18, v2
	v_mad_u64_u32 v[68:69], s[12:13], v68, s14, v[100:101]
	v_lshl_add_u64 v[70:71], v[68:69], 0, s[16:17]
	v_lshl_add_u64 v[68:69], v[68:69], 0, s[18:19]
	v_lshl_add_u64 v[88:89], v[70:71], 0, v[84:85]
	v_lshl_add_u64 v[70:71], v[70:71], 0, v[86:87]
	v_lshl_add_u64 v[88:89], v[68:69], 0, v[84:85]
	v_lshl_add_u64 v[68:69], v[68:69], 0, v[86:87]
	v_or_b32_e32 v68, 19, v2
	v_mad_u64_u32 v[68:69], s[12:13], v68, s14, v[100:101]
	v_lshl_add_u64 v[70:71], v[68:69], 0, s[16:17]
	v_lshl_add_u64 v[68:69], v[68:69], 0, s[18:19]
	v_lshl_add_u64 v[88:89], v[70:71], 0, v[84:85]
	v_lshl_add_u64 v[70:71], v[70:71], 0, v[86:87]
	v_lshl_add_u64 v[88:89], v[68:69], 0, v[84:85]
	v_lshlrev_b32_e32 v1, 2, v1
	v_lshl_add_u64 v[68:69], v[68:69], 0, v[86:87]
	v_or_b32_e32 v88, 24, v2
	global_load_dwordx4 v[80:83], v1, s[6:7]
	global_load_dwordx4 v[76:79], v1, s[6:7] offset:32
	global_load_dwordx4 v[72:75], v1, s[6:7] offset:64
	v_ashrrev_i32_e32 v185, 4, v176
	global_load_dwordx4 v[68:71], v1, s[6:7] offset:96
	v_mad_u64_u32 v[88:89], s[6:7], v88, s14, v[100:101]
	v_lshl_add_u64 v[90:91], v[88:89], 0, s[16:17]
	v_lshl_add_u64 v[88:89], v[88:89], 0, s[18:19]
	v_lshl_add_u64 v[92:93], v[90:91], 0, v[84:85]
	v_lshl_add_u64 v[90:91], v[90:91], 0, v[86:87]
	v_lshl_add_u64 v[92:93], v[88:89], 0, v[84:85]
	v_lshl_add_u64 v[88:89], v[88:89], 0, v[86:87]
	v_or_b32_e32 v1, 25, v2
	v_mad_u64_u32 v[88:89], s[6:7], v1, s14, v[100:101]
	v_lshl_add_u64 v[90:91], v[88:89], 0, s[16:17]
	v_lshl_add_u64 v[88:89], v[88:89], 0, s[18:19]
	v_lshl_add_u64 v[92:93], v[90:91], 0, v[84:85]
	v_lshl_add_u64 v[90:91], v[90:91], 0, v[86:87]
	v_lshl_add_u64 v[92:93], v[88:89], 0, v[84:85]
	v_lshl_add_u64 v[88:89], v[88:89], 0, v[86:87]
	v_or_b32_e32 v1, 26, v2
	v_mad_u64_u32 v[88:89], s[6:7], v1, s14, v[100:101]
	v_lshl_add_u64 v[90:91], v[88:89], 0, s[16:17]
	v_lshl_add_u64 v[88:89], v[88:89], 0, s[18:19]
	v_lshl_add_u64 v[92:93], v[90:91], 0, v[84:85]
	v_lshl_add_u64 v[90:91], v[90:91], 0, v[86:87]
	v_lshl_add_u64 v[92:93], v[88:89], 0, v[84:85]
	v_lshl_add_u64 v[88:89], v[88:89], 0, v[86:87]
	v_or_b32_e32 v1, 27, v2
	v_mad_u64_u32 v[88:89], s[6:7], v1, s14, v[100:101]
	v_lshl_add_u64 v[90:91], v[88:89], 0, s[16:17]
	v_lshl_add_u64 v[88:89], v[88:89], 0, s[18:19]
	v_lshl_add_u64 v[92:93], v[90:91], 0, v[84:85]
	v_lshl_add_u64 v[84:85], v[88:89], 0, v[84:85]
	v_lshl_add_u64 v[84:85], v[90:91], 0, v[86:87]
	v_lshl_add_u64 v[84:85], v[88:89], 0, v[86:87]
	v_and_b32_e32 v84, 15, v176
	v_lshlrev_b32_e32 v102, 3, v84
	v_or_b32_e32 v191, s2, v102
	v_lshlrev_b32_e32 v96, 2, v191
	global_load_dwordx4 v[84:87], v96, s[0:1] offset:16
	global_load_dwordx4 v[92:95], v96, s[0:1]
	global_load_dwordx4 v[88:91], v96, s[4:5] offset:16
	s_nop 0
	global_load_dwordx4 v[96:99], v96, s[4:5]
	v_add_u32_e32 v110, s11, v185
	v_readlane_b32 s0, v254, 37
	v_mov_b32_e32 v103, v3
	v_readlane_b32 s1, v254, 38
	v_ashrrev_i32_e32 v111, 31, v110
	v_lshlrev_b64 v[104:105], 7, v[110:111]
	v_lshl_add_u64 v[102:103], s[0:1], 0, v[102:103]
	v_lshl_add_u64 v[112:113], v[102:103], 0, v[104:105]
	global_load_dwordx2 v[104:105], v[112:113], off
	s_movk_i32 s0, 0x2000
	v_add_co_u32_e32 v116, vcc, s0, v112
	s_movk_i32 s0, 0x3000
	s_nop 0
	v_addc_co_u32_e32 v117, vcc, 0, v113, vcc
	global_load_dwordx2 v[102:103], v[116:117], off offset:-4096
	global_load_dwordx2 v[186:187], v[116:117], off
	v_add_co_u32_e32 v112, vcc, s0, v112
	v_and_b32_e32 v106, 64, v229
	s_nop 0
	v_addc_co_u32_e32 v113, vcc, 0, v113, vcc
	v_add_u32_e32 v106, 64, v106
	v_xor_b32_e32 v108, 1, v229
	v_cmp_lt_i32_e32 vcc, v108, v106
	global_load_dwordx2 v[188:189], v[112:113], off
	s_mov_b32 s0, 0x3a800000
	v_cndmask_b32_e32 v108, v229, v108, vcc
	v_lshlrev_b32_e32 v145, 2, v108
	v_xor_b32_e32 v108, 2, v229
	v_cmp_lt_i32_e32 vcc, v108, v106
	s_movk_i32 s4, 0x4000
	v_and_b32_e32 v184, 63, v176
	v_cndmask_b32_e32 v108, v229, v108, vcc
	v_lshlrev_b32_e32 v111, 2, v108
	v_xor_b32_e32 v108, 4, v229
	v_cmp_lt_i32_e32 vcc, v108, v106
	s_cmpk_gt_u32 s10, 0xff
	s_waitcnt vmcnt(3)
; __device__ __forceinline__ void unit(const bf16_t* proj, const float* stats  , const float* lng, const float* lnb, const float* sw, const float* sb, bf16_t* Y2, int un, LAS unsigned char* lds) {
;     ...
;       { float2 pp[4];
; #pragma unroll
;         for (int q = 0; q < 4; ++q) pp[q] = *(const float2*)(stats + ((size_t)(R0 + sr + 32 * q) * 16 + (tid & 15)) * 2);
;         asm volatile("" ::: "memory");
; #pragma unroll
;         for (int q = 0; q < 4; ++q) { float s1 = pp[q].x, s2 = pp[q].y;
; #pragma unroll
;             for (int off = 1; off < 16; off <<= 1) { s1 += __shfl_xor(s1, off); s2 += __shfl_xor(s2, off); }
;             mus[q] = s1 * (1.0f / 1024.0f); rss[q] = __builtin_amdgcn_rsqf(fmaxf(s2 * (1.0f / 1024.0f) - mus[q] * mus[q], 0.f) + LN_EPS); } }
; #pragma unroll
;       for (int q = 0; q < 4; ++q) { const int s = sr + 32 * q, row = R0 + s; const u32x4 vv = *(const u32x4*)(proj + (size_t)row * NC + C_VC + ch);
	v_and_b32_e32 v160, 63, v176
	v_lshlrev_b32_e32 v160, 4, v160
	v_lshrrev_b32_e32 v161, 6, v176
	v_lshl_add_u32 v160, v161, 13, v160
	v_add_u32_e32 v160, 0x10000, v160
	ds_write_b128 v160, v[120:123] offset:0
	ds_write_b128 v160, v[136:139] offset:4096
	ds_write_b128 v160, v[124:127] offset:1024
	ds_write_b128 v160, v[140:143] offset:5120
	ds_write_b128 v160, v[128:131] offset:2048
	ds_write_b128 v160, v[148:151] offset:6144
	ds_write_b128 v160, v[132:135] offset:3072
	ds_write_b128 v160, v[152:155] offset:7168
	ds_bpermute_b32 v112, v145, v104
	ds_bpermute_b32 v113, v145, v105
	v_cndmask_b32_e32 v108, v229, v108, vcc
	v_lshlrev_b32_e32 v190, 2, v108
	v_xor_b32_e32 v108, 8, v229
	v_cmp_lt_i32_e32 vcc, v108, v106
	s_waitcnt lgkmcnt(0)
	v_pk_add_f32 v[104:105], v[104:105], v[112:113]
	ds_bpermute_b32 v112, v111, v104
	ds_bpermute_b32 v113, v111, v105
	v_cndmask_b32_e32 v106, v229, v108, vcc
	v_lshlrev_b32_e32 v106, 2, v106
	s_waitcnt lgkmcnt(0)
	v_pk_add_f32 v[104:105], v[104:105], v[112:113]
	ds_bpermute_b32 v112, v190, v104
	ds_bpermute_b32 v113, v190, v105
	s_waitcnt lgkmcnt(0)
	v_pk_add_f32 v[104:105], v[104:105], v[112:113]
	ds_bpermute_b32 v112, v106, v104
	ds_bpermute_b32 v113, v106, v105
	s_waitcnt lgkmcnt(0)
	v_pk_add_f32 v[104:105], v[104:105], v[112:113]
	s_nop 0
	v_pk_mul_f32 v[116:117], v[104:105], s[0:1] op_sel_hi:[1,0]
	s_waitcnt vmcnt(2)
	ds_bpermute_b32 v105, v145, v103
	v_fma_f32 v104, -v116, v116, v117
	v_max_f32_e32 v104, 0, v104
	v_add_f32_e32 v104, 0x3727c5ac, v104
	v_rsq_f32_e32 v118, v104
	ds_bpermute_b32 v104, v145, v102
	s_waitcnt lgkmcnt(0)
	v_pk_add_f32 v[102:103], v[102:103], v[104:105]
	ds_bpermute_b32 v104, v111, v102
	ds_bpermute_b32 v105, v111, v103
	s_waitcnt lgkmcnt(0)
	v_pk_add_f32 v[102:103], v[102:103], v[104:105]
	ds_bpermute_b32 v104, v190, v102
	ds_bpermute_b32 v105, v190, v103
	s_waitcnt lgkmcnt(0)
	v_pk_add_f32 v[102:103], v[102:103], v[104:105]
	ds_bpermute_b32 v104, v106, v102
	ds_bpermute_b32 v105, v106, v103
	s_waitcnt lgkmcnt(0)
	v_pk_add_f32 v[102:103], v[102:103], v[104:105]
	s_nop 0
	v_pk_mul_f32 v[112:113], v[102:103], s[0:1] op_sel_hi:[1,0]
	s_waitcnt vmcnt(1)
	ds_bpermute_b32 v103, v145, v187
	v_fma_f32 v102, -v112, v112, v113
	v_max_f32_e32 v102, 0, v102
	v_add_f32_e32 v102, 0x3727c5ac, v102
	v_rsq_f32_e32 v114, v102
	ds_bpermute_b32 v102, v145, v186
	s_waitcnt lgkmcnt(0)
	v_pk_add_f32 v[102:103], v[186:187], v[102:103]
	ds_bpermute_b32 v104, v111, v102
	ds_bpermute_b32 v105, v111, v103
	s_waitcnt lgkmcnt(0)
	v_pk_add_f32 v[102:103], v[102:103], v[104:105]
	ds_bpermute_b32 v104, v190, v102
	ds_bpermute_b32 v105, v190, v103
	s_waitcnt lgkmcnt(0)
	v_pk_add_f32 v[102:103], v[102:103], v[104:105]
	ds_bpermute_b32 v104, v106, v102
	ds_bpermute_b32 v105, v106, v103
	s_waitcnt lgkmcnt(0)
	v_pk_add_f32 v[102:103], v[102:103], v[104:105]
	s_nop 0
	v_pk_mul_f32 v[102:103], v[102:103], s[0:1] op_sel_hi:[1,0]
	s_waitcnt vmcnt(0)
	ds_bpermute_b32 v105, v145, v189
	v_fma_f32 v104, -v102, v102, v103
	v_max_f32_e32 v104, 0, v104
	v_add_f32_e32 v104, 0x3727c5ac, v104
	v_rsq_f32_e32 v108, v104
	ds_bpermute_b32 v104, v145, v188
	s_waitcnt lgkmcnt(0)
	v_pk_add_f32 v[104:105], v[188:189], v[104:105]
	ds_bpermute_b32 v186, v111, v104
	ds_bpermute_b32 v187, v111, v105
	v_lshlrev_b32_e32 v111, 1, v185
	v_bfe_u32 v188, v176, 2, 2
	s_waitcnt lgkmcnt(0)
	v_pk_add_f32 v[104:105], v[104:105], v[186:187]
	ds_bpermute_b32 v186, v190, v104
	ds_bpermute_b32 v187, v190, v105
	s_waitcnt lgkmcnt(0)
	v_pk_add_f32 v[104:105], v[104:105], v[186:187]
	ds_bpermute_b32 v186, v106, v104
	ds_bpermute_b32 v187, v106, v105
	s_waitcnt lgkmcnt(0)
	v_pk_add_f32 v[104:105], v[104:105], v[186:187]
	v_and_b32_e32 v187, 8, v111
	v_lshrrev_b32_e32 v111, 1, v185
	v_and_b32_e32 v186, 3, v185
	v_and_or_b32 v111, v111, 4, v186
	v_pk_mul_f32 v[104:105], v[104:105], s[0:1] op_sel_hi:[1,0]
	v_lshlrev_b32_e32 v189, 6, v111
	v_mad_i64_i32 v[192:193], s[0:1], v110, s14, v[100:101]
	v_lshlrev_b32_e32 v110, 1, v191
	v_mov_b32_e32 v111, v3
	v_lshl_add_u64 v[192:193], v[192:193], 0, v[110:111]
	v_add_co_u32_e32 v192, vcc, s4, v192
	v_lshlrev_b32_e32 v186, 4, v176
	s_nop 0
	v_addc_co_u32_e32 v193, vcc, 0, v193, vcc
	global_load_dwordx4 v[196:199], v[192:193], off offset:2048
	s_mov_b64 s[100:101], 0x1d0000
	v_lshl_add_u64 v[132:133], v[192:193], 0, s[100:101]
	global_load_dwordx4 v[120:123], v[132:133], off offset:2048
	v_lshl_add_u64 v[132:133], v[132:133], 0, s[100:101]
	global_load_dwordx4 v[124:127], v[132:133], off offset:2048
	v_lshl_add_u64 v[132:133], v[132:133], 0, s[100:101]
	global_load_dwordx4 v[128:131], v[132:133], off offset:2048
	v_and_b32_e32 v190, 48, v186
	v_fma_f32 v106, -v104, v104, v105
	v_max_f32_e32 v106, 0, v106
	v_add_f32_e32 v106, 0x3727c5ac, v106
	v_rsq_f32_e32 v106, v106
	s_waitcnt vmcnt(0)
; __device__ __forceinline__ unsigned cvt_pk_bf16(float lo, float hi) { f32x2_t v = {lo, hi}; bf16x2_t b = __builtin_convertvector(v, bf16x2_t); return __builtin_bit_cast(unsigned, b); }
; #define LAS __attribute__((address_space(3)))
; __device__ __forceinline__ float bflo(unsigned w) { return __uint_as_float(w << 16); }
; __device__ __forceinline__ float bfhi(unsigned w) { return __uint_as_float(w & 0xffff0000u); }
; __device__ __forceinline__ int v_st(int k, int c) { const int kk = (k & ~0xC) | ((k & 4) << 1) | ((k & 8) >> 1); return ((kk >> 3) * 4 + (c >> 5)) * 512 + ((kk & 7) * 32 + (c & 31)) * 2; }
; __device__ __forceinline__ void unit(const bf16_t* proj, const float* stats  , const float* lng, const float* lnb, const float* sw, const float* sb, bf16_t* Y2, int un, LAS unsigned char* lds) {
;     ...
;       for (int q = 0; q < 4; ++q) { const int s = sr + 32 * q, row = R0 + s; const u32x4 vv = *(const u32x4*)(proj + (size_t)row * NC + C_VC + ch);
;           const float mu = mus[q], rs = rss[q];
;           u32x4 w; w.x = pg8::cvt_pk_bf16((bflo(vv.x) - mu) * rs * g0[0] + b0[0], (bfhi(vv.x) - mu) * rs * g0[1] + b0[1]); w.y = pg8::cvt_pk_bf16((bflo(vv.y) - mu) * rs * g0[2] + b0[2], (bfhi(vv.y) - mu) * rs * g0[3] + b0[3]);
;           w.z = pg8::cvt_pk_bf16((bflo(vv.z) - mu) * rs * g1[0] + b1[0], (bfhi(vv.z) - mu) * rs * g1[1] + b1[1]); w.w = pg8::cvt_pk_bf16((bflo(vv.w) - mu) * rs * g1[2] + b1[2], (bfhi(vv.w) - mu) * rs * g1[3] + b1[3]);
;           *(LAS u32x4*)(lds + (s >> 6) * att::SHM_V + att::v_st(s & 63, sc)) = w; } }
	v_lshlrev_b32_e32 v192, 16, v196
	v_and_b32_e32 v193, 0xffff0000, v196
	v_pk_add_f32 v[192:193], v[192:193], v[116:117] op_sel_hi:[1,0] neg_lo:[0,1] neg_hi:[0,1]
	s_nop 0
	v_pk_mul_f32 v[192:193], v[118:119], v[192:193] op_sel_hi:[0,1]
	v_pk_fma_f32 v[192:193], v[92:93], v[192:193], v[96:97]
	s_nop 0
	v_cvt_pk_bf16_f32 v196, v192, v193
	v_lshlrev_b32_e32 v192, 16, v197
	v_and_b32_e32 v193, 0xffff0000, v197
	v_pk_add_f32 v[192:193], v[192:193], v[116:117] op_sel_hi:[1,0] neg_lo:[0,1] neg_hi:[0,1]
	s_nop 0
	v_pk_mul_f32 v[192:193], v[118:119], v[192:193] op_sel_hi:[0,1]
	v_pk_fma_f32 v[192:193], v[94:95], v[192:193], v[98:99]
	s_nop 0
	v_cvt_pk_bf16_f32 v197, v192, v193
	v_lshlrev_b32_e32 v192, 16, v198
	v_and_b32_e32 v193, 0xffff0000, v198
	v_pk_add_f32 v[192:193], v[192:193], v[116:117] op_sel_hi:[1,0] neg_lo:[0,1] neg_hi:[0,1]
	s_nop 0
	v_pk_mul_f32 v[192:193], v[118:119], v[192:193] op_sel_hi:[0,1]
	v_pk_fma_f32 v[192:193], v[84:85], v[192:193], v[88:89]
	s_nop 0
	v_cvt_pk_bf16_f32 v198, v192, v193
	v_lshlrev_b32_e32 v192, 16, v199
	v_and_b32_e32 v193, 0xffff0000, v199
	v_pk_add_f32 v[116:117], v[192:193], v[116:117] op_sel_hi:[1,0] neg_lo:[0,1] neg_hi:[0,1]
	s_nop 0
	v_pk_mul_f32 v[116:117], v[118:119], v[116:117] op_sel_hi:[0,1]
	v_pk_fma_f32 v[116:117], v[86:87], v[116:117], v[90:91]
	s_nop 0
	v_cvt_pk_bf16_f32 v199, v116, v117
	v_lshlrev_b32_e32 v116, 8, v185
	v_and_b32_e32 v117, 0xffffc000, v116
	v_and_or_b32 v116, v185, 48, v187
	v_lshrrev_b32_e32 v116, 1, v116
	v_or_b32_e32 v116, v116, v188
	v_lshlrev_b32_e32 v116, 9, v116
	v_add3_u32 v117, 0, v117, v116
	v_add3_u32 v117, v117, v189, v190
	ds_write_b128 v117, v[196:199]
	v_add_u32_e32 v117, 32, v185
	v_add_u32_e32 v118, s11, v117
	v_mad_i64_i32 v[192:193], s[0:1], v118, s14, v[100:101]
	v_lshl_add_u64 v[192:193], v[192:193], 0, v[110:111]
	v_add_co_u32_e32 v192, vcc, s4, v192
	s_nop 1
	v_addc_co_u32_e32 v193, vcc, 0, v193, vcc
	v_mov_b32_e32 v196, v120
	v_mov_b32_e32 v197, v121
	v_mov_b32_e32 v198, v122
	v_mov_b32_e32 v199, v123
	s_waitcnt vmcnt(0)
	v_lshlrev_b32_e32 v192, 16, v196
	v_and_b32_e32 v193, 0xffff0000, v196
	v_pk_add_f32 v[192:193], v[192:193], v[112:113] op_sel_hi:[1,0] neg_lo:[0,1] neg_hi:[0,1]
	s_nop 0
	v_pk_mul_f32 v[192:193], v[114:115], v[192:193] op_sel_hi:[0,1]
	v_pk_fma_f32 v[192:193], v[92:93], v[192:193], v[96:97]
	s_nop 0
	v_cvt_pk_bf16_f32 v196, v192, v193
	v_lshlrev_b32_e32 v192, 16, v197
	v_and_b32_e32 v193, 0xffff0000, v197
	v_pk_add_f32 v[192:193], v[192:193], v[112:113] op_sel_hi:[1,0] neg_lo:[0,1] neg_hi:[0,1]
	s_nop 0
	v_pk_mul_f32 v[192:193], v[114:115], v[192:193] op_sel_hi:[0,1]
	v_pk_fma_f32 v[192:193], v[94:95], v[192:193], v[98:99]
	s_nop 0
	v_cvt_pk_bf16_f32 v197, v192, v193
	v_lshlrev_b32_e32 v192, 16, v198
	v_and_b32_e32 v193, 0xffff0000, v198
	v_pk_add_f32 v[192:193], v[192:193], v[112:113] op_sel_hi:[1,0] neg_lo:[0,1] neg_hi:[0,1]
	s_nop 0
	v_pk_mul_f32 v[192:193], v[114:115], v[192:193] op_sel_hi:[0,1]
	v_pk_fma_f32 v[192:193], v[84:85], v[192:193], v[88:89]
	s_nop 0
	v_cvt_pk_bf16_f32 v198, v192, v193
	v_lshlrev_b32_e32 v192, 16, v199
	v_and_b32_e32 v193, 0xffff0000, v199
	v_pk_add_f32 v[112:113], v[192:193], v[112:113] op_sel_hi:[1,0] neg_lo:[0,1] neg_hi:[0,1]
	s_nop 0
	v_pk_mul_f32 v[112:113], v[114:115], v[112:113] op_sel_hi:[0,1]
	v_pk_fma_f32 v[112:113], v[86:87], v[112:113], v[90:91]
	v_add_u32_e32 v114, 64, v185
	v_cvt_pk_bf16_f32 v199, v112, v113
	v_and_or_b32 v113, v117, 48, v187
	v_lshrrev_b32_e32 v113, 1, v113
	v_lshlrev_b32_e32 v112, 8, v117
	v_or_b32_e32 v113, v113, v188
	v_and_b32_e32 v112, 0xffffc000, v112
	v_lshlrev_b32_e32 v113, 9, v113
	v_add3_u32 v112, 0, v112, v113
	v_add3_u32 v112, v112, v189, v190
	ds_write_b128 v112, v[196:199]
	v_add_u32_e32 v112, s11, v114
	v_mad_i64_i32 v[112:113], s[0:1], v112, s14, v[100:101]
	v_lshl_add_u64 v[112:113], v[112:113], 0, v[110:111]
	v_add_co_u32_e32 v112, vcc, s4, v112
	s_nop 1
	v_addc_co_u32_e32 v113, vcc, 0, v113, vcc
	v_mov_b32_e32 v196, v124
	v_mov_b32_e32 v197, v125
	v_mov_b32_e32 v198, v126
	v_mov_b32_e32 v199, v127
	s_waitcnt vmcnt(0)
	v_lshlrev_b32_e32 v112, 16, v196
	v_and_b32_e32 v113, 0xffff0000, v196
	v_pk_add_f32 v[112:113], v[112:113], v[102:103] op_sel_hi:[1,0] neg_lo:[0,1] neg_hi:[0,1]
	s_nop 0
	v_pk_mul_f32 v[112:113], v[108:109], v[112:113] op_sel_hi:[0,1]
	v_pk_fma_f32 v[112:113], v[92:93], v[112:113], v[96:97]
	s_nop 0
	v_cvt_pk_bf16_f32 v196, v112, v113
	v_lshlrev_b32_e32 v112, 16, v197
	v_and_b32_e32 v113, 0xffff0000, v197
	v_pk_add_f32 v[112:113], v[112:113], v[102:103] op_sel_hi:[1,0] neg_lo:[0,1] neg_hi:[0,1]
	s_nop 0
	v_pk_mul_f32 v[112:113], v[108:109], v[112:113] op_sel_hi:[0,1]
	v_pk_fma_f32 v[112:113], v[94:95], v[112:113], v[98:99]
	s_nop 0
	v_cvt_pk_bf16_f32 v197, v112, v113
	v_lshlrev_b32_e32 v112, 16, v198
	v_and_b32_e32 v113, 0xffff0000, v198
	v_pk_add_f32 v[112:113], v[112:113], v[102:103] op_sel_hi:[1,0] neg_lo:[0,1] neg_hi:[0,1]
	s_nop 0
	v_pk_mul_f32 v[112:113], v[108:109], v[112:113] op_sel_hi:[0,1]
	v_pk_fma_f32 v[112:113], v[84:85], v[112:113], v[88:89]
	s_nop 0
	v_cvt_pk_bf16_f32 v198, v112, v113
	v_lshlrev_b32_e32 v112, 16, v199
	v_and_b32_e32 v113, 0xffff0000, v199
	v_pk_add_f32 v[102:103], v[112:113], v[102:103] op_sel_hi:[1,0] neg_lo:[0,1] neg_hi:[0,1]
	s_nop 0
	v_pk_mul_f32 v[102:103], v[108:109], v[102:103] op_sel_hi:[0,1]
	v_pk_fma_f32 v[102:103], v[86:87], v[102:103], v[90:91]
	v_add_u32_e32 v108, 0x60, v185
	v_cvt_pk_bf16_f32 v199, v102, v103
	v_lshlrev_b32_e32 v102, 8, v114
	v_and_b32_e32 v102, 0xffffc000, v102
	v_add3_u32 v102, 0, v102, v116
	v_add3_u32 v102, v102, v189, v190
	ds_write_b128 v102, v[196:199]
	v_add_u32_e32 v102, s11, v108
	v_mad_i64_i32 v[100:101], s[0:1], v102, s14, v[100:101]
	v_lshl_add_u64 v[100:101], v[100:101], 0, v[110:111]
	v_add_co_u32_e32 v100, vcc, s4, v100
	s_cselect_b64 s[0:1], -1, 0
	s_nop 0
	v_addc_co_u32_e32 v101, vcc, 0, v101, vcc
	v_mov_b32_e32 v100, v128
	v_mov_b32_e32 v101, v129
	v_mov_b32_e32 v102, v130
	v_mov_b32_e32 v103, v131
	v_cmp_le_u32_e32 vcc, v183, v182
	s_mov_b64 s[4:5], -1
	s_waitcnt vmcnt(0)
; __device__ __forceinline__ unsigned cvt_pk_bf16(float lo, float hi) { f32x2_t v = {lo, hi}; bf16x2_t b = __builtin_convertvector(v, bf16x2_t); return __builtin_bit_cast(unsigned, b); }
; #define LAS __attribute__((address_space(3)))
; __device__ __forceinline__ float bflo(unsigned w) { return __uint_as_float(w << 16); }
; __device__ __forceinline__ float bfhi(unsigned w) { return __uint_as_float(w & 0xffff0000u); }
; __device__ __forceinline__ int crow(int r, int hi) { return (r & 3) + 8 * (r >> 2) + 4 * hi; }
; __device__ __forceinline__ int v_st(int k, int c) { const int kk = (k & ~0xC) | ((k & 4) << 1) | ((k & 8) >> 1); return ((kk >> 3) * 4 + (c >> 5)) * 512 + ((kk & 7) * 32 + (c & 31)) * 2; }
; __device__ __forceinline__ void unit(const bf16_t* proj, const float* stats  , const float* lng, const float* lnb, const float* sw, const float* sb, bf16_t* Y2, int un, LAS unsigned char* lds) {
;     ...
;     for (int r = 0; r < 16; ++r) { const int tr = tb * 32 + att::crow(r, hi), bt = R0 + tr; bias[r] = sb[g * 128 + tr];
; #pragma unroll
;         for (int d = 0; d < 2; ++d) { const int ch = g * 128 + (2 * eh + d) * 32 + (r32 & ~1); uu[r * 2 + d] = *(const unsigned*)(proj + (size_t)bt * NC + C_UC + ch); zq[r * 2 + d] = *(const unsigned*)(proj + (size_t)bt * NC + C_ZC + ch); } }
;     ...
;       for (int q = 0; q < 4; ++q) { const int s = sr + 32 * q, row = R0 + s; const u32x4 vv = *(const u32x4*)(proj + (size_t)row * NC + C_VC + ch);
;           const float mu = mus[q], rs = rss[q];
;           u32x4 w; w.x = pg8::cvt_pk_bf16((bflo(vv.x) - mu) * rs * g0[0] + b0[0], (bfhi(vv.x) - mu) * rs * g0[1] + b0[1]); w.y = pg8::cvt_pk_bf16((bflo(vv.y) - mu) * rs * g0[2] + b0[2], (bfhi(vv.y) - mu) * rs * g0[3] + b0[3]);
;           w.z = pg8::cvt_pk_bf16((bflo(vv.z) - mu) * rs * g1[0] + b1[0], (bfhi(vv.z) - mu) * rs * g1[1] + b1[1]); w.w = pg8::cvt_pk_bf16((bflo(vv.w) - mu) * rs * g1[2] + b1[2], (bfhi(vv.w) - mu) * rs * g1[3] + b1[3]);
;           *(LAS u32x4*)(lds + (s >> 6) * att::SHM_V + att::v_st(s & 63, sc)) = w; } }
;     __syncthreads();
	v_lshlrev_b32_e32 v110, 16, v100
	v_and_b32_e32 v111, 0xffff0000, v100
	v_pk_add_f32 v[110:111], v[110:111], v[104:105] op_sel_hi:[1,0] neg_lo:[0,1] neg_hi:[0,1]
	v_cndmask_b32_e32 v32, 0, v32, vcc
	v_pk_mul_f32 v[110:111], v[106:107], v[110:111] op_sel_hi:[0,1]
	v_pk_fma_f32 v[92:93], v[92:93], v[110:111], v[96:97]
	v_lshlrev_b32_e32 v96, 16, v101
	v_and_b32_e32 v97, 0xffff0000, v101
	v_pk_add_f32 v[96:97], v[96:97], v[104:105] op_sel_hi:[1,0] neg_lo:[0,1] neg_hi:[0,1]
	v_cvt_pk_bf16_f32 v92, v92, v93
	v_pk_mul_f32 v[96:97], v[106:107], v[96:97] op_sel_hi:[0,1]
	v_pk_fma_f32 v[94:95], v[94:95], v[96:97], v[98:99]
	v_cmp_lt_u32_e32 vcc, v183, v182
	v_cvt_pk_bf16_f32 v93, v94, v95
	v_lshlrev_b32_e32 v94, 16, v102
	v_and_b32_e32 v95, 0xffff0000, v102
	v_pk_add_f32 v[94:95], v[94:95], v[104:105] op_sel_hi:[1,0] neg_lo:[0,1] neg_hi:[0,1]
	v_cndmask_b32_e32 v33, 0, v33, vcc
	v_pk_mul_f32 v[94:95], v[106:107], v[94:95] op_sel_hi:[0,1]
	v_pk_fma_f32 v[84:85], v[84:85], v[94:95], v[88:89]
	s_nop 0
	v_cvt_pk_bf16_f32 v94, v84, v85
	v_lshlrev_b32_e32 v84, 16, v103
	v_and_b32_e32 v85, 0xffff0000, v103
	v_pk_add_f32 v[84:85], v[84:85], v[104:105] op_sel_hi:[1,0] neg_lo:[0,1] neg_hi:[0,1]
	s_nop 0
	v_pk_mul_f32 v[84:85], v[106:107], v[84:85] op_sel_hi:[0,1]
	v_pk_fma_f32 v[84:85], v[86:87], v[84:85], v[90:91]
	v_and_b32_e32 v86, 0xc0, v186
	v_cvt_pk_bf16_f32 v95, v84, v85
	v_and_or_b32 v85, v108, 48, v187
	v_lshrrev_b32_e32 v85, 1, v85
	v_lshlrev_b32_e32 v84, 8, v108
	v_or_b32_e32 v85, v85, v188
	v_and_b32_e32 v84, 0xffffc000, v84
	v_lshlrev_b32_e32 v85, 9, v85
	v_add3_u32 v84, 0, v84, v85
	v_add3_u32 v84, v84, v189, v190
	ds_write_b128 v84, v[92:95]
	v_lshlrev_b32_e32 v84, 3, v184
	v_and_b32_e32 v85, 24, v84
	v_lshlrev_b32_e32 v87, 1, v176
	v_and_b32_e32 v87, 32, v87
	v_and_b32_e32 v84, 0x100, v84
	v_add3_u32 v85, 0, v85, v86
	v_add3_u32 v100, v85, v87, v84
	v_or_b32_e32 v84, 2, v183
	v_cmp_le_u32_e32 vcc, v84, v182
	v_or_b32_e32 v84, 3, v183
	v_lshrrev_b32_e32 v161, 6, v176
	v_and_b32_e32 v162, 30, v176
	v_lshlrev_b32_e32 v162, 1, v162
	v_bfe_u32 v163, v176, 5, 1
	v_lshl_add_u32 v162, v163, 9, v162
	v_lshl_add_u32 v162, v161, 13, v162
	v_add_u32_e32 v162, 0x10000, v162
	ds_read_b32 v180, v162 offset:0
	ds_read_b32 v178, v162 offset:64
	ds_read_b32 v181, v162 offset:4096
	ds_read_b32 v179, v162 offset:4160
	ds_read_b32 v173, v162 offset:128
	ds_read_b32 v172, v162 offset:192
	ds_read_b32 v174, v162 offset:4288
	ds_read_b32 v175, v162 offset:4224
	ds_read_b32 v170, v162 offset:256
	ds_read_b32 v168, v162 offset:320
	ds_read_b32 v169, v162 offset:4416
	ds_read_b32 v171, v162 offset:4352
	ds_read_b32 v165, v162 offset:384
	ds_read_b32 v164, v162 offset:448
	ds_read_b32 v166, v162 offset:4544
	ds_read_b32 v167, v162 offset:4480
	ds_read_b32 v157, v162 offset:1152
	ds_read_b32 v156, v162 offset:1216
	ds_read_b32 v158, v162 offset:5312
	ds_read_b32 v159, v162 offset:5248
	ds_read_b32 v154, v162 offset:1280
	ds_read_b32 v152, v162 offset:1344
	ds_read_b32 v153, v162 offset:5440
	ds_read_b32 v155, v162 offset:5376
	ds_read_b32 v149, v162 offset:1408
	ds_read_b32 v148, v162 offset:1472
	ds_read_b32 v150, v162 offset:5568
	ds_read_b32 v151, v162 offset:5504
	ds_read_b32 v146, v162 offset:2048
	ds_read_b32 v143, v162 offset:2112
	ds_read_b32 v144, v162 offset:6208
	ds_read_b32 v147, v162 offset:6144
	ds_read_b32 v140, v162 offset:2176
	ds_read_b32 v139, v162 offset:2240
	ds_read_b32 v141, v162 offset:6336
	ds_read_b32 v142, v162 offset:6272
	ds_read_b32 v137, v162 offset:2304
	ds_read_b32 v135, v162 offset:2368
	ds_read_b32 v136, v162 offset:6464
	ds_read_b32 v138, v162 offset:6400
	ds_read_b32 v133, v162 offset:2432
	ds_read_b32 v131, v162 offset:2496
	ds_read_b32 v134, v162 offset:6528
	ds_read_b32 v132, v162 offset:6592
	ds_read_b32 v129, v162 offset:3072
	ds_read_b32 v127, v162 offset:3136
	ds_read_b32 v128, v162 offset:7232
	ds_read_b32 v130, v162 offset:7168
	ds_read_b32 v125, v162 offset:3200
	ds_read_b32 v123, v162 offset:3264
	ds_read_b32 v124, v162 offset:7360
	ds_read_b32 v126, v162 offset:7296
	ds_read_b32 v121, v162 offset:3328
	ds_read_b32 v119, v162 offset:3392
	ds_read_b32 v120, v162 offset:7488
	ds_read_b32 v122, v162 offset:7424
	ds_read_b32 v109, v162 offset:3456
	ds_read_b32 v115, v162 offset:7552
	ds_read_b32 v1, v162 offset:3520
	ds_read_b32 v107, v162 offset:7616
	ds_read_b32 v160, v162 offset:1088
	ds_read_b32 v161, v162 offset:5184
	ds_read_b32 v163, v162 offset:5120
	ds_read_b32 v162, v162 offset:1024
	s_waitcnt lgkmcnt(0)
	v_cndmask_b32_e32 v34, 0, v34, vcc
	v_cmp_le_u32_e32 vcc, v84, v182
	v_or_b32_e32 v84, 4, v183
	s_barrier
; __device__ __forceinline__ unsigned cvt_pk_bf16(float lo, float hi) { f32x2_t v = {lo, hi}; bf16x2_t b = __builtin_convertvector(v, bf16x2_t); return __builtin_bit_cast(unsigned, b); }
; __device__ __forceinline__ void unit(const bf16_t* proj, const float* stats  , const float* lng, const float* lnb, const float* sw, const float* sb, bf16_t* Y2, int un, LAS unsigned char* lds) {
;     ...
;         if (st * 64 > tb * 32 + 31) continue;
;         att::bf16x8 pa[4];
; #pragma unroll
;         for (int k = 0; k < 4; ++k) { const int s0 = st * 64 + 16 * k + hi * 8; const f32x4 w0 = wv[2 * (st * 4 + k)], w1 = wv[2 * (st * 4 + k) + 1];
;             float x[8] = {w0[0], w0[1], w0[2], w0[3], w1[0], w1[1], w1[2], w1[3]};
; #pragma unroll
;             for (int j = 0; j < 8; ++j) x[j] = (s0 + j <= t) ? x[j] : 0.f;
;             u32x4 p; p.x = pg8::cvt_pk_bf16(x[0], x[1]); p.y = pg8::cvt_pk_bf16(x[2], x[3]); p.z = pg8::cvt_pk_bf16(x[4], x[5]); p.w = pg8::cvt_pk_bf16(x[6], x[7]); pa[k] = __builtin_bit_cast(att::bf16x8, p); }
;         if (eh == 0) { att::pv_one<0>(o0, vb + st * att::SHM_V, pa[0], pa[1], pa[2], pa[3]); att::pv_one<1>(o1, vb + st * att::SHM_V, pa[0], pa[1], pa[2], pa[3]); }
;         else         { att::pv_one<2>(o0, vb + st * att::SHM_V, pa[0], pa[1], pa[2], pa[3]); att::pv_one<3>(o1, vb + st * att::SHM_V, pa[0], pa[1], pa[2], pa[3]); }
	v_cndmask_b32_e32 v35, 0, v35, vcc
	v_cmp_le_u32_e32 vcc, v84, v182
	v_or_b32_e32 v84, 5, v183
	v_cvt_pk_bf16_f32 v85, v34, v35
	v_cndmask_b32_e32 v28, 0, v28, vcc
	v_cmp_le_u32_e32 vcc, v84, v182
	v_or_b32_e32 v84, 6, v183
	s_nop 0
	v_cndmask_b32_e32 v29, 0, v29, vcc
	v_cmp_le_u32_e32 vcc, v84, v182
	v_or_b32_e32 v84, 7, v183
	v_cvt_pk_bf16_f32 v86, v28, v29
	v_cndmask_b32_e32 v30, 0, v30, vcc
	v_cmp_le_u32_e32 vcc, v84, v182
	v_or_b32_e32 v28, 16, v183
	v_cvt_pk_bf16_f32 v84, v32, v33
	v_cndmask_b32_e32 v31, 0, v31, vcc
	v_cmp_le_u32_e32 vcc, v28, v182
	v_or_b32_e32 v28, 17, v183
	v_cvt_pk_bf16_f32 v87, v30, v31
	v_cndmask_b32_e32 v24, 0, v24, vcc
	v_cmp_le_u32_e32 vcc, v28, v182
	v_or_b32_e32 v28, 18, v183
	s_nop 0
	v_cndmask_b32_e32 v25, 0, v25, vcc
	v_cmp_le_u32_e32 vcc, v28, v182
	v_or_b32_e32 v28, 19, v183
	v_cvt_pk_bf16_f32 v88, v24, v25
	v_cndmask_b32_e32 v26, 0, v26, vcc
	v_cmp_le_u32_e32 vcc, v28, v182
	v_or_b32_e32 v28, 20, v183
	s_nop 0
	v_cndmask_b32_e32 v27, 0, v27, vcc
	v_cmp_le_u32_e32 vcc, v28, v182
	v_or_b32_e32 v28, 21, v183
	v_cvt_pk_bf16_f32 v89, v26, v27
	v_cndmask_b32_e32 v20, 0, v20, vcc
	v_cmp_le_u32_e32 vcc, v28, v182
	v_or_b32_e32 v28, 22, v183
	s_nop 0
	v_cndmask_b32_e32 v21, 0, v21, vcc
	v_cmp_le_u32_e32 vcc, v28, v182
	v_or_b32_e32 v28, 23, v183
	v_cvt_pk_bf16_f32 v90, v20, v21
	v_cndmask_b32_e32 v22, 0, v22, vcc
	v_cmp_le_u32_e32 vcc, v28, v182
	v_or_b32_e32 v20, 32, v183
	s_nop 0
	v_cndmask_b32_e32 v23, 0, v23, vcc
	v_cmp_le_u32_e32 vcc, v20, v182
	v_or_b32_e32 v20, 33, v183
	v_cvt_pk_bf16_f32 v91, v22, v23
	v_cndmask_b32_e32 v16, 0, v16, vcc
	v_cmp_le_u32_e32 vcc, v20, v182
	v_or_b32_e32 v20, 34, v183
	s_nop 0
	v_cndmask_b32_e32 v17, 0, v17, vcc
	v_cmp_le_u32_e32 vcc, v20, v182
	v_or_b32_e32 v20, 35, v183
	v_cvt_pk_bf16_f32 v96, v16, v17
	v_cndmask_b32_e32 v18, 0, v18, vcc
	v_cmp_le_u32_e32 vcc, v20, v182
	v_or_b32_e32 v20, 36, v183
	s_nop 0
	v_cndmask_b32_e32 v19, 0, v19, vcc
	v_cmp_le_u32_e32 vcc, v20, v182
	v_or_b32_e32 v20, 37, v183
	v_cvt_pk_bf16_f32 v97, v18, v19
	v_cndmask_b32_e32 v12, 0, v12, vcc
	v_cmp_le_u32_e32 vcc, v20, v182
	v_or_b32_e32 v20, 38, v183
	s_nop 0
	v_cndmask_b32_e32 v13, 0, v13, vcc
	v_cmp_le_u32_e32 vcc, v20, v182
	v_or_b32_e32 v20, 39, v183
	v_cvt_pk_bf16_f32 v98, v12, v13
	v_cndmask_b32_e32 v14, 0, v14, vcc
	v_cmp_le_u32_e32 vcc, v20, v182
	v_or_b32_e32 v12, 48, v183
	s_nop 0
	v_cndmask_b32_e32 v15, 0, v15, vcc
	v_cmp_le_u32_e32 vcc, v12, v182
	v_or_b32_e32 v12, 49, v183
	v_cvt_pk_bf16_f32 v99, v14, v15
	v_cndmask_b32_e32 v8, 0, v8, vcc
	v_cmp_le_u32_e32 vcc, v12, v182
	v_or_b32_e32 v12, 50, v183
	s_nop 0
	v_cndmask_b32_e32 v9, 0, v9, vcc
	v_cmp_le_u32_e32 vcc, v12, v182
	v_or_b32_e32 v12, 51, v183
	v_cvt_pk_bf16_f32 v92, v8, v9
	v_cndmask_b32_e32 v10, 0, v10, vcc
	v_cmp_le_u32_e32 vcc, v12, v182
	v_or_b32_e32 v12, 52, v183
	s_nop 0
	v_cndmask_b32_e32 v11, 0, v11, vcc
	v_cmp_le_u32_e32 vcc, v12, v182
	v_or_b32_e32 v12, 53, v183
	v_cvt_pk_bf16_f32 v93, v10, v11
	v_cndmask_b32_e32 v4, 0, v4, vcc
	v_cmp_le_u32_e32 vcc, v12, v182
	v_or_b32_e32 v12, 54, v183
	s_nop 0
	v_cndmask_b32_e32 v5, 0, v5, vcc
	v_cmp_le_u32_e32 vcc, v12, v182
	v_or_b32_e32 v12, 55, v183
	v_cvt_pk_bf16_f32 v94, v4, v5
	v_cndmask_b32_e32 v6, 0, v6, vcc
	v_cmp_le_u32_e32 vcc, v12, v182
	s_nop 1
	v_cndmask_b32_e32 v7, 0, v7, vcc
	v_cvt_pk_bf16_f32 v95, v6, v7
	s_and_b64 vcc, exec, s[0:1]
	s_cbranch_vccz .LBB0_1379
	ds_read_b64_tr_b16 v[4:5], v100 offset:1024
	ds_read_b64_tr_b16 v[6:7], v100 offset:3072
	ds_read_b64_tr_b16 v[20:21], v100 offset:5120
	ds_read_b64_tr_b16 v[22:23], v100 offset:7168
	s_mov_b64 s[4:5], 0
	s_waitcnt lgkmcnt(2)
	v_mfma_f32_32x32x16_bf16 v[4:19], v[84:87], v[4:7], 0
	s_waitcnt lgkmcnt(0)
	v_mfma_f32_32x32x16_bf16 v[4:19], v[88:91], v[20:23], v[4:19]
	ds_read_b64_tr_b16 v[20:21], v100 offset:9216
	ds_read_b64_tr_b16 v[22:23], v100 offset:11264
	s_waitcnt lgkmcnt(0)
	v_mfma_f32_32x32x16_bf16 v[4:19], v[96:99], v[20:23], v[4:19]
	ds_read_b64_tr_b16 v[20:21], v100 offset:13312
	ds_read_b64_tr_b16 v[22:23], v100 offset:15360
	s_waitcnt lgkmcnt(0)
	v_mfma_f32_32x32x16_bf16 v[4:19], v[92:95], v[20:23], v[4:19]
	ds_read_b64_tr_b16 v[22:23], v100 offset:3584
	ds_read_b64_tr_b16 v[20:21], v100 offset:1536
	ds_read_b64_tr_b16 v[104:105], v100 offset:7680
	ds_read_b64_tr_b16 v[102:103], v100 offset:5632
	s_waitcnt lgkmcnt(2)
	v_mfma_f32_32x32x16_bf16 v[20:35], v[84:87], v[20:23], 0
	s_waitcnt lgkmcnt(0)
	v_mfma_f32_32x32x16_bf16 v[20:35], v[88:91], v[102:105], v[20:35]
	ds_read_b64_tr_b16 v[104:105], v100 offset:11776
	ds_read_b64_tr_b16 v[102:103], v100 offset:9728
	s_waitcnt lgkmcnt(0)
	v_mfma_f32_32x32x16_bf16 v[20:35], v[96:99], v[102:105], v[20:35]
	ds_read_b64_tr_b16 v[104:105], v100 offset:15872
	ds_read_b64_tr_b16 v[102:103], v100 offset:13824
	s_waitcnt lgkmcnt(0)
	v_mfma_f32_32x32x16_bf16 v[20:35], v[92:95], v[102:105], v[20:35]
